# converter f32 weight loads in the P1 tail and P4 carry sc1 (agent scope) besides nt, to keep them from displacing the GEMM tiles in L2
# speedup vs baseline: 1.0057x; 1.0057x over previous
;     __device__ __forceinline__ CvtDesc desc(int qq) const { return cvt_desc(*F, item_of(qq), qq & 1, h); }
;     __device__ __forceinline__ void proc() { cvt_to_lds(buf, desc(q), img, gl, q & 1, h, F->lane); if (q & 1) fitem = item_of(q); ++q; }
;     __device__ __forceinline__ void flush() { if (fitem >= 0) { cvt_flush(cvt_desc(*F, fitem, 0, h), img, h, F->lane); fitem = -1; } }
; __device__ __forceinline__ void cvt_load(CvtBuf& b, const CvtDesc& d, int lane) {
;     const float* p = d.W + (size_t)(d.k0 + 16 * (lane >> 5)) * d.ldw + d.n0 + 4 * (lane & 31);
; #pragma unroll
;     for (int i = 0; i < 16; ++i) b.v[i] = __builtin_nontemporal_load((const f32x4*)(p + (size_t)i * d.ldw));
; }
;     __device__ __forceinline__ void drain() {
;         __syncthreads(); flush(); __syncthreads();
;         if (state != 0) { proc(); state = 0; if (fitem >= 0) { __syncthreads(); flush(); __syncthreads(); } }
;         if (q >= nq) { __syncthreads(); return; }
;         CvtBuf b2;
;         cvt_load(buf, desc(q), F->lane);
.LBB0_292:
	v_readlane_b32 s7, v254, 8
	s_bfe_u32 s7, s7, 0x10006
	s_lshl_b32 s10, s10, 7
	s_lshl_b32 s11, s7, 6
	v_lshrrev_b32_e32 v2, 1, v0
	s_and_b32 s10, s10, 0x780
	v_and_or_b32 v131, v2, 16, s11
	v_or_b32_e32 v2, s10, v131
	v_mul_u32_u24_e32 v2, s6, v2
	v_lshlrev_b32_e32 v132, 2, v2
	v_mov_b32_e32 v133, 0
	s_mov_b32 s5, 0
	s_lshl_b32 s4, s4, 7
	v_lshl_add_u64 v[2:3], s[0:1], 0, v[132:133]
	v_and_b32_e32 v130, 0x7c, v130
	v_lshl_add_u64 v[2:3], s[4:5], 2, v[2:3]
	v_lshlrev_b32_e32 v132, 2, v130
	v_lshl_add_u64 v[10:11], v[2:3], 0, v[132:133]
	s_lshl_b32 s4, s6, 2
	v_lshl_add_u64 v[12:13], v[10:11], 0, s[4:5]
	v_lshl_add_u64 v[18:19], v[12:13], 0, s[4:5]
	v_lshl_add_u64 v[20:21], v[18:19], 0, s[4:5]
	v_lshl_add_u64 v[26:27], v[20:21], 0, s[4:5]
	v_lshl_add_u64 v[28:29], v[26:27], 0, s[4:5]
	v_lshl_add_u64 v[34:35], v[28:29], 0, s[4:5]
	v_lshl_add_u64 v[36:37], v[34:35], 0, s[4:5]
	v_lshl_add_u64 v[38:39], v[36:37], 0, s[4:5]
	v_lshl_add_u64 v[42:43], v[38:39], 0, s[4:5]
	v_lshl_add_u64 v[46:47], v[42:43], 0, s[4:5]
	v_lshl_add_u64 v[50:51], v[46:47], 0, s[4:5]
	v_lshl_add_u64 v[54:55], v[50:51], 0, s[4:5]
	v_lshl_add_u64 v[58:59], v[54:55], 0, s[4:5]
	v_lshl_add_u64 v[62:63], v[58:59], 0, s[4:5]
	global_load_dwordx4 v[2:5], v[10:11], off sc1 nt
	global_load_dwordx4 v[6:9], v[12:13], off sc1 nt
	s_nop 0
	global_load_dwordx4 v[10:13], v[18:19], off sc1 nt
	global_load_dwordx4 v[14:17], v[20:21], off sc1 nt
	s_nop 0
	global_load_dwordx4 v[18:21], v[26:27], off sc1 nt
	global_load_dwordx4 v[22:25], v[28:29], off sc1 nt
	s_nop 0
	global_load_dwordx4 v[26:29], v[34:35], off sc1 nt
	global_load_dwordx4 v[30:33], v[36:37], off sc1 nt
	v_readlane_b32 s0, v254, 47
	global_load_dwordx4 v[34:37], v[38:39], off sc1 nt
	s_lshl_b32 s0, s0, 13
	global_load_dwordx4 v[38:41], v[42:43], off sc1 nt
	s_and_b32 s0, s0, 0x7fffc000
	global_load_dwordx4 v[42:45], v[46:47], off sc1 nt
	s_add_i32 s1, 0, 0x16000
	global_load_dwordx4 v[46:49], v[50:51], off sc1 nt
	s_lshl_b32 s6, s7, 8
	global_load_dwordx4 v[50:53], v[54:55], off sc1 nt
	s_add_i32 s6, s6, 0
	global_load_dwordx4 v[54:57], v[58:59], off sc1 nt
	s_lshl_b32 s10, s7, 2
	global_load_dwordx4 v[58:61], v[62:63], off sc1 nt
	v_lshl_add_u64 v[62:63], v[62:63], 0, s[4:5]
	global_load_dwordx4 v[62:65], v[62:63], off sc1 nt
	s_add_i32 s4, s1, s0
	s_add_u32 s39, s30, 0x50000000
	v_lshlrev_b32_e32 v68, 9, v0
	s_addc_u32 s40, s31, 0
	v_lshrrev_b32_e32 v66, 5, v190
	v_and_b32_e32 v68, 0x3e00, v68
	s_add_u32 s41, s30, 0x30000000
	v_or_b32_e32 v67, s10, v66
	v_add_u32_e32 v68, s4, v68
	v_and_b32_e32 v69, 7, v0
	s_addc_u32 s42, s31, 0
	v_lshrrev_b32_e32 v71, 3, v190
	s_lshl_b32 s4, s7, 13
	v_bitop3_b32 v70, s10, v69, v66 bitop3:0x36
	v_bitop3_b32 v67, v67, v69, 2 bitop3:0x36
	v_or_b32_e32 v140, s11, v71
	s_or_b32 s0, s0, s4
	v_lshlrev_b32_e32 v70, 4, v70
	v_lshlrev_b32_e32 v72, 7, v71
	v_lshlrev_b32_e32 v67, 4, v67
	v_or_b32_e32 v141, 24, v140
	s_add_i32 s1, s1, s0
	v_or_b32_e32 v144, 16, v140
	v_or_b32_e32 v146, 8, v140
	v_and_b32_e32 v134, 0x70, v1
	v_mov_b32_e32 v135, v133
	v_and_b32_e32 v1, 0x80, v72
	v_or_b32_e32 v138, 32, v131
	v_lshl_add_u32 v139, v66, 6, s6
	v_lshrrev_b32_e32 v142, 2, v141
	v_add_u32_e32 v143, s1, v72
	v_lshrrev_b32_e32 v145, 2, v144
	v_lshrrev_b32_e32 v147, 2, v146
	v_lshrrev_b32_e32 v148, 2, v140
	v_add_u32_e32 v149, v68, v70
	v_add_u32_e32 v150, v68, v67
	v_mov_b32_e32 v151, 0x42800000
	s_mov_b32 s43, 0
	s_branch .LBB0_294

; __device__ __forceinline__ void cvt_load(CvtBuf& b, const CvtDesc& d, int lane) {
;     const float* p = d.W + (size_t)(d.k0 + 16 * (lane >> 5)) * d.ldw + d.n0 + 4 * (lane & 31);
; #pragma unroll
;     for (int i = 0; i < 16; ++i) b.v[i] = __builtin_nontemporal_load((const f32x4*)(p + (size_t)i * d.ldw));
; }
.LBB0_299:
	s_lshl_b32 s11, s36, 7
	s_and_b32 s11, s11, 0x780
	v_or_b32_e32 v66, s11, v138
	v_mul_u32_u24_e32 v66, s10, v66
	v_lshlrev_b32_e32 v132, 2, v66
	s_lshl_b32 s4, s4, 7
	v_lshl_add_u64 v[66:67], s[0:1], 0, v[132:133]
	v_lshl_add_u64 v[66:67], s[4:5], 2, v[66:67]
	v_lshlrev_b32_e32 v132, 2, v130
	v_lshl_add_u64 v[74:75], v[66:67], 0, v[132:133]
	s_lshl_b32 s4, s10, 2
	v_lshl_add_u64 v[76:77], v[74:75], 0, s[4:5]
	v_lshl_add_u64 v[82:83], v[76:77], 0, s[4:5]
	v_lshl_add_u64 v[84:85], v[82:83], 0, s[4:5]
	v_lshl_add_u64 v[90:91], v[84:85], 0, s[4:5]
	v_lshl_add_u64 v[92:93], v[90:91], 0, s[4:5]
	v_lshl_add_u64 v[98:99], v[92:93], 0, s[4:5]
	v_lshl_add_u64 v[100:101], v[98:99], 0, s[4:5]
	v_lshl_add_u64 v[102:103], v[100:101], 0, s[4:5]
	v_lshl_add_u64 v[106:107], v[102:103], 0, s[4:5]
	v_lshl_add_u64 v[110:111], v[106:107], 0, s[4:5]
	v_lshl_add_u64 v[114:115], v[110:111], 0, s[4:5]
	v_lshl_add_u64 v[118:119], v[114:115], 0, s[4:5]
	v_lshl_add_u64 v[122:123], v[118:119], 0, s[4:5]
	v_lshl_add_u64 v[126:127], v[122:123], 0, s[4:5]
	global_load_dwordx4 v[70:73], v[74:75], off sc1 nt
	global_load_dwordx4 v[66:69], v[76:77], off sc1 nt
	global_load_dwordx4 v[78:81], v[82:83], off sc1 nt
	s_nop 0
	global_load_dwordx4 v[74:77], v[84:85], off sc1 nt
	global_load_dwordx4 v[86:89], v[90:91], off sc1 nt
	s_nop 0
	global_load_dwordx4 v[82:85], v[92:93], off sc1 nt
	global_load_dwordx4 v[94:97], v[98:99], off sc1 nt
	s_nop 0
	global_load_dwordx4 v[90:93], v[100:101], off sc1 nt
	s_nop 0
	global_load_dwordx4 v[98:101], v[102:103], off sc1 nt
	s_nop 0
	global_load_dwordx4 v[102:105], v[106:107], off sc1 nt
	s_nop 0
	global_load_dwordx4 v[106:109], v[110:111], off sc1 nt
	s_nop 0
	global_load_dwordx4 v[110:113], v[114:115], off sc1 nt
	s_nop 0
	global_load_dwordx4 v[114:117], v[118:119], off sc1 nt
	s_nop 0
	global_load_dwordx4 v[118:121], v[122:123], off sc1 nt
	s_nop 0
	global_load_dwordx4 v[122:125], v[126:127], off sc1 nt
	v_lshl_add_u64 v[126:127], v[126:127], 0, s[4:5]
	global_load_dwordx4 v[126:129], v[126:127], off sc1 nt

; __device__ __forceinline__ void cvt_load(CvtBuf& b, const CvtDesc& d, int lane) {
;     const float* p = d.W + (size_t)(d.k0 + 16 * (lane >> 5)) * d.ldw + d.n0 + 4 * (lane & 31);
; #pragma unroll
;     for (int i = 0; i < 16; ++i) b.v[i] = __builtin_nontemporal_load((const f32x4*)(p + (size_t)i * d.ldw));
; }
.LBB0_306:
	s_lshl_b32 s15, s45, 7
	s_and_b32 s15, s15, 0x780
	v_or_b32_e32 v2, s15, v131
	v_mul_u32_u24_e32 v2, s14, v2
	v_lshlrev_b32_e32 v132, 2, v2
	s_lshl_b32 s4, s4, 7
	v_lshl_add_u64 v[2:3], s[10:11], 0, v[132:133]
	v_lshl_add_u64 v[2:3], s[4:5], 2, v[2:3]
	v_lshlrev_b32_e32 v132, 2, v130
	v_lshl_add_u64 v[2:3], v[2:3], 0, v[132:133]
	s_lshl_b32 s4, s14, 2
	v_lshl_add_u64 v[10:11], v[2:3], 0, s[4:5]
	global_load_dwordx4 v[2:5], v[2:3], off sc1 nt
	s_nop 0
	global_load_dwordx4 v[6:9], v[10:11], off sc1 nt
	v_lshl_add_u64 v[10:11], v[10:11], 0, s[4:5]
	v_lshl_add_u64 v[18:19], v[10:11], 0, s[4:5]
	global_load_dwordx4 v[10:13], v[10:11], off sc1 nt
	s_nop 0
	global_load_dwordx4 v[14:17], v[18:19], off sc1 nt
	v_lshl_add_u64 v[18:19], v[18:19], 0, s[4:5]
	v_lshl_add_u64 v[26:27], v[18:19], 0, s[4:5]
	global_load_dwordx4 v[18:21], v[18:19], off sc1 nt
	s_nop 0
	global_load_dwordx4 v[22:25], v[26:27], off sc1 nt
	v_lshl_add_u64 v[26:27], v[26:27], 0, s[4:5]
	v_lshl_add_u64 v[34:35], v[26:27], 0, s[4:5]
	v_lshl_add_u64 v[38:39], v[34:35], 0, s[4:5]
	v_lshl_add_u64 v[42:43], v[38:39], 0, s[4:5]
	v_lshl_add_u64 v[46:47], v[42:43], 0, s[4:5]
	v_lshl_add_u64 v[50:51], v[46:47], 0, s[4:5]
	v_lshl_add_u64 v[54:55], v[50:51], 0, s[4:5]
	v_lshl_add_u64 v[58:59], v[54:55], 0, s[4:5]
	v_lshl_add_u64 v[62:63], v[58:59], 0, s[4:5]
	global_load_dwordx4 v[26:29], v[26:27], off sc1 nt
	s_nop 0
	global_load_dwordx4 v[30:33], v[34:35], off sc1 nt
	s_nop 0
	global_load_dwordx4 v[34:37], v[38:39], off sc1 nt
	s_nop 0
	global_load_dwordx4 v[38:41], v[42:43], off sc1 nt
	s_nop 0
	global_load_dwordx4 v[42:45], v[46:47], off sc1 nt
	s_nop 0
	global_load_dwordx4 v[46:49], v[50:51], off sc1 nt
	s_nop 0
	global_load_dwordx4 v[50:53], v[54:55], off sc1 nt
	s_nop 0
	global_load_dwordx4 v[54:57], v[58:59], off sc1 nt
	s_nop 0
	global_load_dwordx4 v[58:61], v[62:63], off sc1 nt
	v_lshl_add_u64 v[62:63], v[62:63], 0, s[4:5]
	global_load_dwordx4 v[62:65], v[62:63], off sc1 nt
	s_waitcnt vmcnt(16)

;     __device__ __forceinline__ CvtDesc desc(int qq) const { return cvt_desc(*F, item_of(qq), qq & 1, h); }
;     __device__ __forceinline__ void proc() { cvt_to_lds(buf, desc(q), img, gl, q & 1, h, F->lane); if (q & 1) fitem = item_of(q); ++q; }
;     __device__ __forceinline__ void flush() { if (fitem >= 0) { cvt_flush(cvt_desc(*F, fitem, 0, h), img, h, F->lane); fitem = -1; } }
; __device__ __forceinline__ CvtDesc cvt_desc(const Frame& F, int item, int sub2, int h) {
;     CvtDesc d; int kblk, nblk;
;     if (item < CVT_ITEMS1) { const int e = item >> 9, rem = item & 511; kblk = rem >> 5; nblk = rem & 31; d.W = F.w_mlp1 + (size_t)e * DM * 2 * DE; d.ldw = 2 * DE; d.WT = F.ws + WS_W1 + (size_t)e * 2 * DE * DM; d.map = 2; }
;     else { const int it = item - CVT_ITEMS1; const int e = it >> 8, rem = it & 255; kblk = rem >> 4; nblk = rem & 15; d.W = F.w_mlp2 + (size_t)e * DE * DM; d.ldw = DM; d.WT = F.ws + WS_W2 + (size_t)e * DM * DE; d.map = 0; }
;     d.n0 = nblk * 128; d.kb0 = kblk * 128; d.k0 = d.kb0 + 64 * h + 32 * sub2;
;     return d;
; }
; __device__ __forceinline__ void cvt_load(CvtBuf& b, const CvtDesc& d, int lane) {
;     const float* p = d.W + (size_t)(d.k0 + 16 * (lane >> 5)) * d.ldw + d.n0 + 4 * (lane & 31);
; #pragma unroll
;     for (int i = 0; i < 16; ++i) b.v[i] = __builtin_nontemporal_load((const f32x4*)(p + (size_t)i * d.ldw));
; }
;     __device__ __forceinline__ void drain() {
;         __syncthreads(); flush(); __syncthreads();
;         if (state != 0) { proc(); state = 0; if (fitem >= 0) { __syncthreads(); flush(); __syncthreads(); } }
;         if (q >= nq) { __syncthreads(); return; }
;         CvtBuf b2;
;         cvt_load(buf, desc(q), F->lane);
;         while (q < nq) {
.LBB0_902:
	v_readlane_b32 s7, v254, 8
	s_bfe_u32 s7, s7, 0x10006
	s_lshl_b32 s12, s12, 7
	s_lshl_b32 s13, s7, 6
	s_and_b32 s12, s12, 0x780
	v_and_or_b32 v131, v148, 16, s13
	v_or_b32_e32 v2, s12, v131
	v_mul_u32_u24_e32 v2, s6, v2
	v_lshlrev_b32_e32 v132, 2, v2
	v_mov_b32_e32 v133, 0
	s_mov_b32 s5, 0
	s_lshl_b32 s4, s4, 7
	v_lshl_add_u64 v[2:3], s[0:1], 0, v[132:133]
	v_and_b32_e32 v130, 0x7c, v130
	v_lshl_add_u64 v[2:3], s[4:5], 2, v[2:3]
	v_lshlrev_b32_e32 v132, 2, v130
	v_lshl_add_u64 v[10:11], v[2:3], 0, v[132:133]
	s_lshl_b32 s4, s6, 2
	v_lshl_add_u64 v[12:13], v[10:11], 0, s[4:5]
	v_lshl_add_u64 v[18:19], v[12:13], 0, s[4:5]
	v_lshl_add_u64 v[20:21], v[18:19], 0, s[4:5]
	v_lshl_add_u64 v[26:27], v[20:21], 0, s[4:5]
	v_lshl_add_u64 v[28:29], v[26:27], 0, s[4:5]
	v_lshl_add_u64 v[34:35], v[28:29], 0, s[4:5]
	v_lshl_add_u64 v[36:37], v[34:35], 0, s[4:5]
	v_lshl_add_u64 v[38:39], v[36:37], 0, s[4:5]
	v_lshl_add_u64 v[42:43], v[38:39], 0, s[4:5]
	v_lshl_add_u64 v[46:47], v[42:43], 0, s[4:5]
	v_lshl_add_u64 v[50:51], v[46:47], 0, s[4:5]
	v_lshl_add_u64 v[54:55], v[50:51], 0, s[4:5]
	v_lshl_add_u64 v[58:59], v[54:55], 0, s[4:5]
	v_lshl_add_u64 v[62:63], v[58:59], 0, s[4:5]
	global_load_dwordx4 v[2:5], v[10:11], off sc1 nt
	global_load_dwordx4 v[6:9], v[12:13], off sc1 nt
	s_nop 0
	global_load_dwordx4 v[10:13], v[18:19], off sc1 nt
	global_load_dwordx4 v[14:17], v[20:21], off sc1 nt
	s_nop 0
	global_load_dwordx4 v[18:21], v[26:27], off sc1 nt
	global_load_dwordx4 v[22:25], v[28:29], off sc1 nt
	s_nop 0
	global_load_dwordx4 v[26:29], v[34:35], off sc1 nt
	global_load_dwordx4 v[30:33], v[36:37], off sc1 nt
	v_readlane_b32 s0, v254, 47
	global_load_dwordx4 v[34:37], v[38:39], off sc1 nt
	s_lshl_b32 s0, s0, 13
	global_load_dwordx4 v[38:41], v[42:43], off sc1 nt
	s_and_b32 s0, s0, 0x7fffc000
	global_load_dwordx4 v[42:45], v[46:47], off sc1 nt
	s_add_i32 s1, 0, 0x16000
	global_load_dwordx4 v[46:49], v[50:51], off sc1 nt
	s_lshl_b32 s6, s7, 8
	global_load_dwordx4 v[50:53], v[54:55], off sc1 nt
	s_add_i32 s6, s6, 0
	global_load_dwordx4 v[54:57], v[58:59], off sc1 nt
	s_lshl_b32 s12, s7, 2
	global_load_dwordx4 v[58:61], v[62:63], off sc1 nt
	v_lshl_add_u64 v[62:63], v[62:63], 0, s[4:5]
	global_load_dwordx4 v[62:65], v[62:63], off sc1 nt
	s_add_i32 s4, s1, s0
	s_add_u32 s39, s30, 0x50000000
	v_lshlrev_b32_e32 v68, 9, v0
	s_addc_u32 s40, s31, 0
	v_lshrrev_b32_e32 v66, 5, v190
	v_and_b32_e32 v68, 0x3e00, v68
	s_add_u32 s41, s30, 0x30000000
	v_or_b32_e32 v67, s12, v66
	v_add_u32_e32 v68, s4, v68
	v_and_b32_e32 v69, 7, v0
	s_addc_u32 s42, s31, 0
	v_lshrrev_b32_e32 v71, 3, v190
	s_lshl_b32 s4, s7, 13
	v_bitop3_b32 v70, s12, v69, v66 bitop3:0x36
	v_bitop3_b32 v67, v67, v69, 2 bitop3:0x36
	v_or_b32_e32 v141, s13, v71
	s_or_b32 s0, s0, s4
	v_lshlrev_b32_e32 v70, 4, v70
	v_lshlrev_b32_e32 v72, 7, v71
	v_lshlrev_b32_e32 v67, 4, v67
	v_or_b32_e32 v142, 24, v141
	s_add_i32 s1, s1, s0
	v_or_b32_e32 v145, 16, v141
	v_or_b32_e32 v147, 8, v141
	v_and_b32_e32 v134, 0x70, v1
	v_mov_b32_e32 v135, v133
	v_and_b32_e32 v138, 0x80, v72
	v_or_b32_e32 v139, 32, v131
	v_lshl_add_u32 v140, v66, 6, s6
	v_lshrrev_b32_e32 v143, 2, v142
	v_add_u32_e32 v144, s1, v72
	v_lshrrev_b32_e32 v146, 2, v145
	v_lshrrev_b32_e32 v148, 2, v147
	v_lshrrev_b32_e32 v149, 2, v141
	v_add_u32_e32 v150, v68, v70
	v_add_u32_e32 v151, v68, v67
	v_mov_b32_e32 v152, 0x42800000
	s_mov_b32 s43, 0
	s_branch .LBB0_904

; __device__ __forceinline__ void cvt_load(CvtBuf& b, const CvtDesc& d, int lane) {
;     const float* p = d.W + (size_t)(d.k0 + 16 * (lane >> 5)) * d.ldw + d.n0 + 4 * (lane & 31);
; #pragma unroll
;     for (int i = 0; i < 16; ++i) b.v[i] = __builtin_nontemporal_load((const f32x4*)(p + (size_t)i * d.ldw));
; }
.LBB0_909:
	s_lshl_b32 s13, s36, 7
	s_and_b32 s13, s13, 0x780
	v_or_b32_e32 v66, s13, v139
	v_mul_u32_u24_e32 v66, s12, v66
	v_lshlrev_b32_e32 v132, 2, v66
	s_lshl_b32 s4, s4, 7
	v_lshl_add_u64 v[66:67], s[0:1], 0, v[132:133]
	v_lshl_add_u64 v[66:67], s[4:5], 2, v[66:67]
	v_lshlrev_b32_e32 v132, 2, v130
	v_lshl_add_u64 v[74:75], v[66:67], 0, v[132:133]
	s_lshl_b32 s4, s12, 2
	v_lshl_add_u64 v[76:77], v[74:75], 0, s[4:5]
	v_lshl_add_u64 v[82:83], v[76:77], 0, s[4:5]
	v_lshl_add_u64 v[84:85], v[82:83], 0, s[4:5]
	v_lshl_add_u64 v[90:91], v[84:85], 0, s[4:5]
	v_lshl_add_u64 v[92:93], v[90:91], 0, s[4:5]
	v_lshl_add_u64 v[98:99], v[92:93], 0, s[4:5]
	v_lshl_add_u64 v[100:101], v[98:99], 0, s[4:5]
	v_lshl_add_u64 v[102:103], v[100:101], 0, s[4:5]
	v_lshl_add_u64 v[106:107], v[102:103], 0, s[4:5]
	v_lshl_add_u64 v[110:111], v[106:107], 0, s[4:5]
	v_lshl_add_u64 v[114:115], v[110:111], 0, s[4:5]
	v_lshl_add_u64 v[118:119], v[114:115], 0, s[4:5]
	v_lshl_add_u64 v[122:123], v[118:119], 0, s[4:5]
	v_lshl_add_u64 v[126:127], v[122:123], 0, s[4:5]
	global_load_dwordx4 v[70:73], v[74:75], off sc1 nt
	global_load_dwordx4 v[66:69], v[76:77], off sc1 nt
	global_load_dwordx4 v[78:81], v[82:83], off sc1 nt
	s_nop 0
	global_load_dwordx4 v[74:77], v[84:85], off sc1 nt
	global_load_dwordx4 v[86:89], v[90:91], off sc1 nt
	s_nop 0
	global_load_dwordx4 v[82:85], v[92:93], off sc1 nt
	global_load_dwordx4 v[94:97], v[98:99], off sc1 nt
	s_nop 0
	global_load_dwordx4 v[90:93], v[100:101], off sc1 nt
	s_nop 0
	global_load_dwordx4 v[98:101], v[102:103], off sc1 nt
	s_nop 0
	global_load_dwordx4 v[102:105], v[106:107], off sc1 nt
	s_nop 0
	global_load_dwordx4 v[106:109], v[110:111], off sc1 nt
	s_nop 0
	global_load_dwordx4 v[110:113], v[114:115], off sc1 nt
	s_nop 0
	global_load_dwordx4 v[114:117], v[118:119], off sc1 nt
	s_nop 0
	global_load_dwordx4 v[118:121], v[122:123], off sc1 nt
	s_nop 0
	global_load_dwordx4 v[122:125], v[126:127], off sc1 nt
	v_lshl_add_u64 v[126:127], v[126:127], 0, s[4:5]
	global_load_dwordx4 v[126:129], v[126:127], off sc1 nt

; __device__ __forceinline__ void cvt_load(CvtBuf& b, const CvtDesc& d, int lane) {
;     const float* p = d.W + (size_t)(d.k0 + 16 * (lane >> 5)) * d.ldw + d.n0 + 4 * (lane & 31);
; #pragma unroll
;     for (int i = 0; i < 16; ++i) b.v[i] = __builtin_nontemporal_load((const f32x4*)(p + (size_t)i * d.ldw));
; }
.LBB0_916:
	s_lshl_b32 s15, s45, 7
	s_and_b32 s15, s15, 0x780
	v_or_b32_e32 v2, s15, v131
	v_mul_u32_u24_e32 v2, s14, v2
	v_lshlrev_b32_e32 v132, 2, v2
	s_lshl_b32 s4, s4, 7
	v_lshl_add_u64 v[2:3], s[12:13], 0, v[132:133]
	v_lshl_add_u64 v[2:3], s[4:5], 2, v[2:3]
	v_lshlrev_b32_e32 v132, 2, v130
	v_lshl_add_u64 v[10:11], v[2:3], 0, v[132:133]
	s_lshl_b32 s4, s14, 2
	v_lshl_add_u64 v[12:13], v[10:11], 0, s[4:5]
	v_lshl_add_u64 v[18:19], v[12:13], 0, s[4:5]
	v_lshl_add_u64 v[20:21], v[18:19], 0, s[4:5]
	v_lshl_add_u64 v[26:27], v[20:21], 0, s[4:5]
	v_lshl_add_u64 v[28:29], v[26:27], 0, s[4:5]
	v_lshl_add_u64 v[34:35], v[28:29], 0, s[4:5]
	v_lshl_add_u64 v[36:37], v[34:35], 0, s[4:5]
	v_lshl_add_u64 v[38:39], v[36:37], 0, s[4:5]
	v_lshl_add_u64 v[42:43], v[38:39], 0, s[4:5]
	v_lshl_add_u64 v[46:47], v[42:43], 0, s[4:5]
	v_lshl_add_u64 v[50:51], v[46:47], 0, s[4:5]
	v_lshl_add_u64 v[54:55], v[50:51], 0, s[4:5]
	v_lshl_add_u64 v[58:59], v[54:55], 0, s[4:5]
	v_lshl_add_u64 v[62:63], v[58:59], 0, s[4:5]
	global_load_dwordx4 v[2:5], v[10:11], off sc1 nt
	global_load_dwordx4 v[6:9], v[12:13], off sc1 nt
	s_nop 0
	global_load_dwordx4 v[10:13], v[18:19], off sc1 nt
	global_load_dwordx4 v[14:17], v[20:21], off sc1 nt
	s_nop 0
	global_load_dwordx4 v[18:21], v[26:27], off sc1 nt
	global_load_dwordx4 v[22:25], v[28:29], off sc1 nt
	s_nop 0
	global_load_dwordx4 v[26:29], v[34:35], off sc1 nt
	global_load_dwordx4 v[30:33], v[36:37], off sc1 nt
	s_nop 0
	global_load_dwordx4 v[34:37], v[38:39], off sc1 nt
	s_nop 0
	global_load_dwordx4 v[38:41], v[42:43], off sc1 nt
	s_nop 0
	global_load_dwordx4 v[42:45], v[46:47], off sc1 nt
	s_nop 0
	global_load_dwordx4 v[46:49], v[50:51], off sc1 nt
	s_nop 0
	global_load_dwordx4 v[50:53], v[54:55], off sc1 nt
	s_nop 0
	global_load_dwordx4 v[54:57], v[58:59], off sc1 nt
	s_nop 0
	global_load_dwordx4 v[58:61], v[62:63], off sc1 nt
	v_lshl_add_u64 v[62:63], v[62:63], 0, s[4:5]
	global_load_dwordx4 v[62:65], v[62:63], off sc1 nt
	s_waitcnt vmcnt(16)
